# speedup vs baseline: 1.0099x; 1.0099x over previous
_Z11prep_kernelPKfPKiS0_S0_S0_PiP15HIP_vector_typeIjLj2EEP6OvfRecPDF16_S9_S9_:
	s_mov_b32 s33, s2
	s_cmpk_lt_u32 s2, 0x80
	s_movk_i32 s3, 0x7a2
	s_cselect_b32 s26, s3, 0xffffff80
	s_add_i32 s26, s26, s2
	s_cmpk_gt_i32 s26, 0x186
	s_mov_b64 s[2:3], -1
	s_cbranch_scc0 .LBB0_29
	s_cmpk_gt_u32 s26, 0x7a1
	v_bfe_u32 v1, v0, 3, 2
	s_cbranch_scc0 .LBB0_19
	s_cmpk_lt_u32 s26, 0x7e2
	s_load_dwordx4 s[4:7], s[0:1], 0x48
	s_load_dwordx4 s[8:11], s[0:1], 0x18
	s_cselect_b64 s[2:3], -1, 0
	s_cmpk_gt_u32 s26, 0x7e1
	s_cselect_b64 s[12:13], -1, 0
	s_lshl_b32 s18, s26, 10
	s_addk_i32 s18, 0x7800
	s_bfe_u32 s17, s18, 0x4000c
	s_lshr_b32 s14, s18, 8
	v_bfe_u32 v4, v0, 3, 4
	v_lshrrev_b32_e32 v3, 2, v0
	s_and_b32 s16, s14, 0xc0
	s_lshl_b32 s19, s17, 4
	s_and_b64 vcc, exec, s[12:13]
	s_cbranch_vccz .LBB0_4
	s_and_b32 s14, s19, 48
	s_or_b32 s14, s14, s16
	v_or_b32_e32 v2, s14, v4
	s_and_b32 s18, s18, 0xfc00
	v_and_b32_e32 v5, 24, v3
	s_cbranch_execz .LBB0_5
	s_branch .LBB0_6

.LBB0_37:
	s_or_b64 exec, exec, s[4:5]
	s_load_dwordx4 s[12:15], s[0:1], 0x8
	v_lshl_or_b32 v3, s26, 11, v0
	s_mov_b32 s6, 0xc3500
	v_mov_b32_e32 v1, 0xc34ff
	v_cmp_gt_i32_e64 s[4:5], s6, v3
	s_waitcnt lgkmcnt(0)
	s_bfe_u32 s36, s33, 0x20001
	s_mul_i32 s37, s36, 0x1400
	s_add_u32 s22, s22, s37
	s_addc_u32 s23, s23, 0
	s_lshl_b32 s36, s36, 2
	s_addk_i32 s36, 0x800
	s_add_u32 s36, s20, s36
	s_addc_u32 s37, s21, 0
	s_barrier
	v_cndmask_b32_e64 v4, v1, v3, s[4:5]
	v_ashrrev_i32_e32 v5, 31, v4
	v_lshlrev_b64 v[4:5], 2, v[4:5]
	v_lshl_add_u64 v[6:7], s[12:13], 0, v[4:5]
	v_add_co_u32_e32 v8, vcc, 0x30d000, v6
	v_lshl_add_u64 v[4:5], s[14:15], 0, v[4:5]
	s_nop 0
	v_addc_co_u32_e32 v9, vcc, 0, v7, vcc
	global_load_dword v19, v[8:9], off offset:1024 nt
	global_load_dword v30, v[6:7], off nt
	global_load_dword v32, v[4:5], off nt
	v_min_i32_e32 v4, 0xc33ff, v3
	v_ashrrev_i32_e32 v5, 31, v4
	v_lshlrev_b64 v[4:5], 2, v[4:5]
	s_mov_b32 s7, 0x30d000
	v_lshl_add_u64 v[6:7], s[12:13], 0, v[4:5]
	v_add_co_u32_e32 v8, vcc, s7, v6
	v_lshl_add_u64 v[4:5], s[14:15], 0, v[4:5]
	s_nop 0
	v_addc_co_u32_e32 v9, vcc, 0, v7, vcc
	global_load_dword v13, v[8:9], off offset:2048 nt
	global_load_dword v26, v[6:7], off offset:1024 nt
	global_load_dword v28, v[4:5], off offset:1024 nt
	v_min_i32_e32 v4, 0xc32ff, v3
	v_ashrrev_i32_e32 v5, 31, v4
	v_lshlrev_b64 v[4:5], 2, v[4:5]
	v_lshl_add_u64 v[6:7], s[12:13], 0, v[4:5]
	v_add_co_u32_e32 v8, vcc, s7, v6
	v_lshl_add_u64 v[4:5], s[14:15], 0, v[4:5]
	s_nop 0
	v_addc_co_u32_e32 v9, vcc, 0, v7, vcc
	global_load_dword v11, v[8:9], off offset:3072 nt
	global_load_dword v22, v[6:7], off offset:2048 nt
	global_load_dword v24, v[4:5], off offset:2048 nt
	v_min_i32_e32 v4, 0xc31ff, v3
	v_ashrrev_i32_e32 v5, 31, v4
	v_lshlrev_b64 v[6:7], 2, v[4:5]
	v_lshl_add_u64 v[8:9], s[12:13], 0, v[6:7]
	s_mov_b32 s0, 0x30e000
	v_add_co_u32_e32 v14, vcc, s0, v8
	v_or_b32_e32 v2, 0x400, v3
	s_nop 0
	v_addc_co_u32_e32 v15, vcc, 0, v9, vcc
	v_lshl_add_u64 v[6:7], s[14:15], 0, v[6:7]
	v_cmp_gt_i32_e64 s[0:1], s6, v2
	global_load_dword v5, v[14:15], off nt
	global_load_dword v18, v[8:9], off offset:3072 nt
	global_load_dword v20, v[6:7], off offset:3072 nt
	v_cndmask_b32_e64 v6, v1, v2, s[0:1]
	v_ashrrev_i32_e32 v7, 31, v6
	v_lshlrev_b64 v[8:9], 2, v[6:7]
	v_lshl_add_u64 v[16:17], s[12:13], 0, v[8:9]
	v_add_co_u32_e32 v34, vcc, s7, v16
	v_or_b32_e32 v2, 0x500, v3
	s_nop 0
	v_addc_co_u32_e32 v35, vcc, 0, v17, vcc
	v_lshl_add_u64 v[8:9], s[14:15], 0, v[8:9]
	v_cmp_gt_i32_e64 s[2:3], s6, v2
	global_load_dword v7, v[34:35], off offset:1024 nt
	global_load_dword v14, v[16:17], off nt
	v_mov_b32_e32 v29, 0
	global_load_dword v16, v[8:9], off nt
	v_cndmask_b32_e64 v8, v1, v2, s[2:3]
	v_ashrrev_i32_e32 v9, 31, v8
	v_lshlrev_b64 v[34:35], 2, v[8:9]
	v_lshl_add_u64 v[36:37], s[12:13], 0, v[34:35]
	v_add_co_u32_e32 v38, vcc, s7, v36
	v_or_b32_e32 v2, 0x600, v3
	s_nop 0
	v_addc_co_u32_e32 v39, vcc, 0, v37, vcc
	v_lshl_add_u64 v[34:35], s[14:15], 0, v[34:35]
	v_cmp_gt_i32_e64 s[16:17], s6, v2
	global_load_dword v9, v[38:39], off offset:1024 nt
	global_load_dword v10, v[36:37], off nt
	global_load_dword v12, v[34:35], off nt
	v_cndmask_b32_e64 v34, v1, v2, s[16:17]
	v_ashrrev_i32_e32 v35, 31, v34
	v_lshlrev_b64 v[34:35], 2, v[34:35]
	v_lshl_add_u64 v[36:37], s[12:13], 0, v[34:35]
	v_add_co_u32_e32 v38, vcc, s7, v36
	v_or_b32_e32 v2, 0x700, v3
	s_nop 0
	v_addc_co_u32_e32 v39, vcc, 0, v37, vcc
	v_lshl_add_u64 v[34:35], s[14:15], 0, v[34:35]
	v_cmp_gt_i32_e64 s[18:19], s6, v2
	global_load_dword v33, v[38:39], off offset:1024 nt
	global_load_dword v6, v[36:37], off nt
	global_load_dword v8, v[34:35], off nt
	v_cndmask_b32_e64 v34, v1, v2, s[18:19]
	v_ashrrev_i32_e32 v35, 31, v34
	v_lshlrev_b64 v[36:37], 2, v[34:35]
	v_lshl_add_u64 v[38:39], s[12:13], 0, v[36:37]
	v_add_co_u32_e32 v40, vcc, 0x30d000, v38
	v_lshl_add_u64 v[36:37], s[14:15], 0, v[36:37]
	s_nop 0
	v_addc_co_u32_e32 v41, vcc, 0, v39, vcc
	global_load_dword v34, v[40:41], off offset:1024 nt
	global_load_dword v2, v[38:39], off nt
	global_load_dword v4, v[36:37], off nt
	s_waitcnt vmcnt(23)
	v_cndmask_b32_e64 v31, -1, v19, s[4:5]
	v_cmp_lt_i32_e64 s[14:15], -1, v31
	v_mov_b32_e32 v1, 0
	s_and_saveexec_b64 s[4:5], s[14:15]
	v_lshrrev_b32_e32 v1, 5, v31
	v_and_b32_e32 v1, 0x7fffffc, v1
	v_mov_b32_e32 v15, 1
	ds_add_rtn_u32 v1, v1, v15 offset:1568
	s_or_b64 exec, exec, s[4:5]
	s_mov_b32 s4, 0xc3400
	v_cmp_gt_i32_e32 vcc, s4, v3
	s_waitcnt vmcnt(20)
	s_nop 0
	v_cndmask_b32_e32 v27, -1, v13, vcc
	v_cmp_lt_i32_e64 s[12:13], -1, v27
	s_and_saveexec_b64 s[4:5], s[12:13]
	v_lshrrev_b32_e32 v13, 5, v27
	v_and_b32_e32 v13, 0x7fffffc, v13
	v_mov_b32_e32 v15, 1
	ds_add_rtn_u32 v29, v13, v15 offset:1568
	s_or_b64 exec, exec, s[4:5]
	s_mov_b32 s4, 0xc3300
	v_cmp_gt_i32_e32 vcc, s4, v3
	v_mov_b32_e32 v21, 0
	v_mov_b32_e32 v25, 0
	s_waitcnt vmcnt(17)
	v_cndmask_b32_e32 v23, -1, v11, vcc
	v_cmp_lt_i32_e64 s[10:11], -1, v23
	s_and_saveexec_b64 s[4:5], s[10:11]
	v_lshrrev_b32_e32 v11, 5, v23
	v_and_b32_e32 v11, 0x7fffffc, v11
	v_mov_b32_e32 v13, 1
	ds_add_rtn_u32 v25, v11, v13 offset:1568
	s_or_b64 exec, exec, s[4:5]
	s_mov_b32 s4, 0xc3200
	v_cmp_gt_i32_e32 vcc, s4, v3
	s_waitcnt vmcnt(14)
	s_nop 0
	v_cndmask_b32_e32 v19, -1, v5, vcc
	v_cmp_lt_i32_e64 s[6:7], -1, v19
	s_and_saveexec_b64 s[4:5], s[6:7]
	v_lshrrev_b32_e32 v3, 5, v19
	v_and_b32_e32 v3, 0x7fffffc, v3
	v_mov_b32_e32 v5, 1
	ds_add_rtn_u32 v21, v3, v5 offset:1568
	s_or_b64 exec, exec, s[4:5]
	s_waitcnt vmcnt(11)
	v_cndmask_b32_e64 v15, -1, v7, s[0:1]
	v_cmp_lt_i32_e64 s[4:5], -1, v15
	v_mov_b32_e32 v13, 0
	v_mov_b32_e32 v17, 0
	s_and_saveexec_b64 s[0:1], s[4:5]
	v_lshrrev_b32_e32 v3, 5, v15
	v_and_b32_e32 v3, 0x7fffffc, v3
	v_mov_b32_e32 v5, 1
	ds_add_rtn_u32 v17, v3, v5 offset:1568
	s_or_b64 exec, exec, s[0:1]
	s_waitcnt vmcnt(8)
	v_cndmask_b32_e64 v11, -1, v9, s[2:3]
	v_cmp_lt_i32_e64 s[2:3], -1, v11
	s_and_saveexec_b64 s[0:1], s[2:3]
	v_lshrrev_b32_e32 v3, 5, v11
	v_and_b32_e32 v3, 0x7fffffc, v3
	v_mov_b32_e32 v5, 1
	ds_add_rtn_u32 v13, v3, v5 offset:1568
	s_or_b64 exec, exec, s[0:1]
	s_waitcnt vmcnt(5)
	v_cndmask_b32_e64 v7, -1, v33, s[16:17]
	v_cmp_lt_i32_e64 s[0:1], -1, v7
	v_mov_b32_e32 v5, 0
	v_mov_b32_e32 v9, 0
	s_and_saveexec_b64 s[16:17], s[0:1]
	v_lshrrev_b32_e32 v3, 5, v7
	v_and_b32_e32 v3, 0x7fffffc, v3
	v_mov_b32_e32 v9, 1
	ds_add_rtn_u32 v9, v3, v9 offset:1568
	s_or_b64 exec, exec, s[16:17]
	s_waitcnt vmcnt(2)
	v_cndmask_b32_e64 v3, -1, v34, s[18:19]
	v_cmp_lt_i32_e32 vcc, -1, v3
	s_and_saveexec_b64 s[16:17], vcc
	v_lshrrev_b32_e32 v5, 5, v3
	v_and_b32_e32 v5, 0x7fffffc, v5
	v_mov_b32_e32 v33, 1
	ds_add_rtn_u32 v5, v5, v33 offset:1568
	s_or_b64 exec, exec, s[16:17]
	s_waitcnt lgkmcnt(0)
	s_barrier
	s_and_saveexec_b64 s[16:17], s[8:9]
	s_cbranch_execz .LBB0_58
	s_mul_i32 s28, s26, 61
	s_mov_b64 s[18:19], 0
	s_mov_b32 s29, 0x14f38f63
	s_movk_i32 s30, 0x187
	s_movk_i32 s31, 0x86
	s_branch .LBB0_56

.LBB0_56:
	v_add_u32_e32 v33, s28, v0
	v_mul_hi_i32 v34, v33, s29
	v_lshrrev_b32_e32 v35, 31, v34
	v_ashrrev_i32_e32 v34, 5, v34
	v_add_u32_e32 v34, v34, v35
	v_mul_lo_u32 v34, v34, s30
	v_sub_u32_e32 v34, v33, v34
	v_lshlrev_b32_e32 v33, 2, v34
	ds_read_b32 v36, v33 offset:1568
	v_mov_b32_e32 v35, 0
	s_waitcnt lgkmcnt(0)
	v_cmp_ne_u32_e64 s[8:9], 0, v36
	s_and_saveexec_b64 s[26:27], s[8:9]
	s_cbranch_execz .LBB0_55
	v_lshlrev_b32_e32 v34, 2, v34
	v_ashrrev_i32_e32 v35, 31, v34
	v_lshl_add_u64 v[34:35], v[34:35], 2, s[36:37]
	global_atomic_add v35, v[34:35], v36, off sc0
	s_branch .LBB0_55
.LBB0_58:
	s_or_b64 exec, exec, s[16:17]
	s_waitcnt lgkmcnt(0)
	s_barrier
	s_and_saveexec_b64 s[16:17], s[14:15]
	s_cbranch_execz .LBB0_65
	v_lshrrev_b32_e32 v33, 7, v31
	v_lshlrev_b32_e32 v0, 2, v33
	ds_read_b32 v0, v0
	s_movk_i32 s8, 0x27f
	s_waitcnt lgkmcnt(0)
	v_add_u32_e32 v0, v0, v1
	v_cmp_lt_i32_e64 s[8:9], s8, v0
	s_and_saveexec_b64 s[14:15], s[8:9]
	s_xor_b64 s[14:15], exec, s[14:15]
	s_cbranch_execz .LBB0_63
	s_mov_b64 s[26:27], exec
	v_mbcnt_lo_u32_b32 v0, s26, 0
	v_mbcnt_hi_u32_b32 v0, s27, v0
	v_cmp_eq_u32_e64 s[8:9], 0, v0
	s_and_saveexec_b64 s[18:19], s[8:9]
	s_cbranch_execz .LBB0_62
	s_bcnt1_i32_b64 s8, s[26:27]
	v_mov_b32_e32 v1, 0
	v_mov_b32_e32 v33, s8
	global_atomic_add v1, v1, v33, s[20:21] offset:1600 sc0

.LBB0_65:
	s_or_b64 exec, exec, s[16:17]
	s_and_saveexec_b64 s[14:15], s[12:13]
	s_cbranch_execz .LBB0_72
	v_lshrrev_b32_e32 v30, 7, v27
	v_lshlrev_b32_e32 v0, 2, v30
	ds_read_b32 v0, v0
	s_movk_i32 s8, 0x27f
	s_waitcnt lgkmcnt(0)
	v_add_u32_e32 v0, v0, v29
	v_cmp_lt_i32_e64 s[8:9], s8, v0
	s_and_saveexec_b64 s[12:13], s[8:9]
	s_xor_b64 s[12:13], exec, s[12:13]
	s_cbranch_execz .LBB0_70
	s_mov_b64 s[18:19], exec
	v_mbcnt_lo_u32_b32 v0, s18, 0
	v_mbcnt_hi_u32_b32 v0, s19, v0
	v_cmp_eq_u32_e64 s[8:9], 0, v0
	s_and_saveexec_b64 s[16:17], s[8:9]
	s_cbranch_execz .LBB0_69
	s_bcnt1_i32_b64 s8, s[18:19]
	v_mov_b32_e32 v1, 0
	v_mov_b32_e32 v29, s8
	global_atomic_add v1, v1, v29, s[20:21] offset:1600 sc0

.LBB0_72:
	s_or_b64 exec, exec, s[14:15]
	s_and_saveexec_b64 s[12:13], s[10:11]
	s_cbranch_execz .LBB0_79
	v_lshrrev_b32_e32 v26, 7, v23
	v_lshlrev_b32_e32 v0, 2, v26
	ds_read_b32 v0, v0
	s_movk_i32 s8, 0x27f
	s_waitcnt lgkmcnt(0)
	v_add_u32_e32 v0, v0, v25
	v_cmp_lt_i32_e64 s[8:9], s8, v0
	s_and_saveexec_b64 s[10:11], s[8:9]
	s_xor_b64 s[10:11], exec, s[10:11]
	s_cbranch_execz .LBB0_77
	s_mov_b64 s[16:17], exec
	v_mbcnt_lo_u32_b32 v0, s16, 0
	v_mbcnt_hi_u32_b32 v0, s17, v0
	v_cmp_eq_u32_e64 s[8:9], 0, v0
	s_and_saveexec_b64 s[14:15], s[8:9]
	s_cbranch_execz .LBB0_76
	s_bcnt1_i32_b64 s8, s[16:17]
	v_mov_b32_e32 v1, 0
	v_mov_b32_e32 v25, s8
	global_atomic_add v1, v1, v25, s[20:21] offset:1600 sc0

.LBB0_79:
	s_or_b64 exec, exec, s[12:13]
	s_and_saveexec_b64 s[8:9], s[6:7]
	s_cbranch_execz .LBB0_86
	v_lshrrev_b32_e32 v22, 7, v19
	v_lshlrev_b32_e32 v0, 2, v22
	ds_read_b32 v0, v0
	s_movk_i32 s6, 0x27f
	s_waitcnt lgkmcnt(0)
	v_add_u32_e32 v0, v0, v21
	v_cmp_lt_i32_e64 s[6:7], s6, v0
	s_and_saveexec_b64 s[10:11], s[6:7]
	s_xor_b64 s[10:11], exec, s[10:11]
	s_cbranch_execz .LBB0_84
	s_mov_b64 s[14:15], exec
	v_mbcnt_lo_u32_b32 v0, s14, 0
	v_mbcnt_hi_u32_b32 v0, s15, v0
	v_cmp_eq_u32_e64 s[6:7], 0, v0
	s_and_saveexec_b64 s[12:13], s[6:7]
	s_cbranch_execz .LBB0_83
	s_bcnt1_i32_b64 s6, s[14:15]
	v_mov_b32_e32 v1, 0
	v_mov_b32_e32 v21, s6
	global_atomic_add v1, v1, v21, s[20:21] offset:1600 sc0

.LBB0_86:
	s_or_b64 exec, exec, s[8:9]
	s_and_saveexec_b64 s[6:7], s[4:5]
	s_cbranch_execz .LBB0_93
	v_lshrrev_b32_e32 v18, 7, v15
	v_lshlrev_b32_e32 v0, 2, v18
	ds_read_b32 v0, v0
	s_movk_i32 s4, 0x27f
	s_waitcnt lgkmcnt(0)
	v_add_u32_e32 v0, v0, v17
	v_cmp_lt_i32_e64 s[4:5], s4, v0
	s_and_saveexec_b64 s[8:9], s[4:5]
	s_xor_b64 s[8:9], exec, s[8:9]
	s_cbranch_execz .LBB0_91
	s_mov_b64 s[12:13], exec
	v_mbcnt_lo_u32_b32 v0, s12, 0
	v_mbcnt_hi_u32_b32 v0, s13, v0
	v_cmp_eq_u32_e64 s[4:5], 0, v0
	s_and_saveexec_b64 s[10:11], s[4:5]
	s_cbranch_execz .LBB0_90
	s_bcnt1_i32_b64 s4, s[12:13]
	v_mov_b32_e32 v1, 0
	v_mov_b32_e32 v17, s4
	global_atomic_add v1, v1, v17, s[20:21] offset:1600 sc0

.LBB0_93:
	s_or_b64 exec, exec, s[6:7]
	s_and_saveexec_b64 s[4:5], s[2:3]
	s_cbranch_execz .LBB0_100
	v_lshrrev_b32_e32 v14, 7, v11
	v_lshlrev_b32_e32 v0, 2, v14
	ds_read_b32 v0, v0
	s_movk_i32 s2, 0x27f
	s_waitcnt lgkmcnt(0)
	v_add_u32_e32 v0, v0, v13
	v_cmp_lt_i32_e64 s[2:3], s2, v0
	s_and_saveexec_b64 s[6:7], s[2:3]
	s_xor_b64 s[6:7], exec, s[6:7]
	s_cbranch_execz .LBB0_98
	s_mov_b64 s[10:11], exec
	v_mbcnt_lo_u32_b32 v0, s10, 0
	v_mbcnt_hi_u32_b32 v0, s11, v0
	v_cmp_eq_u32_e64 s[2:3], 0, v0
	s_and_saveexec_b64 s[8:9], s[2:3]
	s_cbranch_execz .LBB0_97
	s_bcnt1_i32_b64 s2, s[10:11]
	v_mov_b32_e32 v1, 0
	v_mov_b32_e32 v13, s2
	global_atomic_add v1, v1, v13, s[20:21] offset:1600 sc0

.LBB0_100:
	s_or_b64 exec, exec, s[4:5]
	s_and_saveexec_b64 s[2:3], s[0:1]
	s_cbranch_execz .LBB0_107
	v_lshrrev_b32_e32 v10, 7, v7
	v_lshlrev_b32_e32 v0, 2, v10
	ds_read_b32 v0, v0
	s_movk_i32 s0, 0x27f
	s_waitcnt lgkmcnt(0)
	v_add_u32_e32 v0, v0, v9
	v_cmp_lt_i32_e64 s[0:1], s0, v0
	s_and_saveexec_b64 s[4:5], s[0:1]
	s_xor_b64 s[4:5], exec, s[4:5]
	s_cbranch_execz .LBB0_105
	s_mov_b64 s[8:9], exec
	v_mbcnt_lo_u32_b32 v0, s8, 0
	v_mbcnt_hi_u32_b32 v0, s9, v0
	v_cmp_eq_u32_e64 s[0:1], 0, v0
	s_and_saveexec_b64 s[6:7], s[0:1]
	s_cbranch_execz .LBB0_104
	s_bcnt1_i32_b64 s0, s[8:9]
	v_mov_b32_e32 v1, 0
	v_mov_b32_e32 v9, s0
	global_atomic_add v1, v1, v9, s[20:21] offset:1600 sc0

.LBB0_107:
	s_or_b64 exec, exec, s[2:3]
	s_and_saveexec_b64 s[0:1], vcc
	s_cbranch_execz .LBB0_115
	v_lshrrev_b32_e32 v6, 7, v3
	v_lshlrev_b32_e32 v0, 2, v6
	ds_read_b32 v0, v0
	s_movk_i32 s0, 0x27f
	s_waitcnt lgkmcnt(0)
	v_add_u32_e32 v0, v0, v5
	v_cmp_lt_i32_e32 vcc, s0, v0
	s_and_saveexec_b64 s[0:1], vcc
	s_xor_b64 s[0:1], exec, s[0:1]
	s_cbranch_execz .LBB0_112
	s_mov_b64 s[4:5], exec
	v_mbcnt_lo_u32_b32 v0, s4, 0
	v_mbcnt_hi_u32_b32 v0, s5, v0
	v_cmp_eq_u32_e32 vcc, 0, v0
	s_and_saveexec_b64 s[2:3], vcc
	s_cbranch_execz .LBB0_111
	s_bcnt1_i32_b64 s4, s[4:5]
	v_mov_b32_e32 v1, 0
	v_mov_b32_e32 v5, s4
	global_atomic_add v1, v1, v5, s[20:21] offset:1600 sc0

	.amdhsa_kernel _Z11prep_kernelPKfPKiS0_S0_S0_PiP15HIP_vector_typeIjLj2EEP6OvfRecPDF16_S9_S9_
		.amdhsa_group_segment_fixed_size 3132
		.amdhsa_private_segment_fixed_size 0
		.amdhsa_kernarg_size 88
		.amdhsa_user_sgpr_count 2
		.amdhsa_user_sgpr_dispatch_ptr 0
		.amdhsa_user_sgpr_queue_ptr 0
		.amdhsa_user_sgpr_kernarg_segment_ptr 1
		.amdhsa_user_sgpr_dispatch_id 0
		.amdhsa_user_sgpr_kernarg_preload_length 0
		.amdhsa_user_sgpr_kernarg_preload_offset 0
		.amdhsa_user_sgpr_private_segment_size 0
		.amdhsa_uses_dynamic_stack 0
		.amdhsa_enable_private_segment 0
		.amdhsa_system_sgpr_workgroup_id_x 1
		.amdhsa_system_sgpr_workgroup_id_y 0
		.amdhsa_system_sgpr_workgroup_id_z 0
		.amdhsa_system_sgpr_workgroup_info 0
		.amdhsa_system_vgpr_workitem_id 0
		.amdhsa_next_free_vgpr 42
		.amdhsa_next_free_sgpr 40
		.amdhsa_accum_offset 44
		.amdhsa_reserve_vcc 1
		.amdhsa_float_round_mode_32 0
		.amdhsa_float_round_mode_16_64 0
		.amdhsa_float_denorm_mode_32 3
		.amdhsa_float_denorm_mode_16_64 3
		.amdhsa_dx10_clamp 1
		.amdhsa_ieee_mode 1
		.amdhsa_fp16_overflow 0
		.amdhsa_tg_split 0
		.amdhsa_exception_fp_ieee_invalid_op 0
		.amdhsa_exception_fp_denorm_src 0
		.amdhsa_exception_fp_ieee_div_zero 0
		.amdhsa_exception_fp_ieee_overflow 0
		.amdhsa_exception_fp_ieee_underflow 0
		.amdhsa_exception_fp_ieee_inexact 0
		.amdhsa_exception_int_div_zero 0
	.end_amdhsa_kernel

_Z13gather_kernelPK15HIP_vector_typeIjLj2EEPKiPK6OvfRecPKDF16_PKfPDF16_:
	s_lshr_b32 s3, s2, 2
	s_and_b32 s3, s3, 0x3ffffffe
	s_and_b32 s4, s2, 1
	s_or_b32 s3, s3, s4
	s_cmpk_gt_u32 s3, 0x186
	s_cbranch_scc1 .LBB1_156
	s_load_dwordx4 s[8:11], s[0:1], 0x0
	s_movk_i32 s4, 0x80
	s_lshl_b32 s12, s3, 4
	s_addk_i32 s12, 0x800
	v_lshrrev_b32_e32 v2, 6, v0
	v_cmp_gt_u32_e64 s[4:5], s4, v0
	v_lshlrev_b32_e32 v1, 2, v0
	v_readfirstlane_b32 s62, v2
	s_and_saveexec_b64 s[6:7], s[4:5]
	v_mov_b32_e32 v2, 0
	ds_write_b32 v1, v2 offset:10832
	s_or_b64 exec, exec, s[6:7]
	s_waitcnt lgkmcnt(0)
	s_load_dwordx4 s[36:39], s[10:11], s12 offset:0x0
	v_cmp_gt_u32_e64 s[6:7], 64, v0
	s_and_saveexec_b64 s[12:13], s[6:7]
	v_mov_b32_e32 v2, 0
	ds_write_b32 v1, v2 offset:11856
	s_or_b64 exec, exec, s[12:13]
	s_waitcnt lgkmcnt(0)
	s_min_u32 s36, s36, 0x280
	s_min_u32 s37, s37, 0x280
	s_min_u32 s38, s38, 0x280
	s_min_u32 s39, s39, 0x280
	s_addk_i32 s37, 0x280
	s_addk_i32 s38, 0x500
	s_addk_i32 s39, 0x780
	s_cmp_ge_u32 s62, 2
	s_cselect_b32 s54, s37, s36
	s_cselect_b32 s59, s39, s38
	s_mov_b32 s52, s36
	s_mov_b32 s53, s36
	s_mov_b32 s55, s37
	s_mov_b32 s56, s37
	s_mov_b32 s57, s38
	s_mov_b32 s58, s38
	s_mov_b32 s60, s39
	s_mov_b32 s61, s39
	s_mul_i32 s15, s3, 0x5000
	s_mul_hi_u32 s13, s3, 0x5000
	s_add_u32 s8, s8, s15
	s_addc_u32 s9, s9, s13
	v_lshlrev_b32_e32 v2, 3, v0
	v_mov_b32_e32 v3, 0
	v_lshl_add_u64 v[4:5], s[8:9], 0, v[2:3]
	s_movk_i32 s13, 0x1000
	s_barrier
	global_load_dwordx2 v[20:21], v2, s[8:9]
	global_load_dwordx2 v[18:19], v2, s[8:9] offset:2048
	v_add_co_u32_e32 v2, vcc, s13, v4
	s_movk_i32 s13, 0x2000
	s_nop 0
	v_addc_co_u32_e32 v3, vcc, 0, v5, vcc
	v_add_co_u32_e32 v6, vcc, s13, v4
	s_movk_i32 s13, 0x3000
	s_nop 0
	v_addc_co_u32_e32 v7, vcc, 0, v5, vcc
	v_add_co_u32_e32 v24, vcc, s13, v4
	v_or_b32_e32 v23, 0x400, v0
	s_nop 0
	v_addc_co_u32_e32 v25, vcc, 0, v5, vcc
	v_lshlrev_b32_e32 v8, 3, v23
	v_or_b32_e32 v22, 0x800, v0
	v_add_co_u32_e32 v26, vcc, 0x4000, v4
	global_load_dwordx2 v[16:17], v[2:3], off
	global_load_dwordx2 v[14:15], v[2:3], off offset:2048
	global_load_dwordx2 v[12:13], v8, s[8:9]
	global_load_dwordx2 v[10:11], v[6:7], off offset:2048
	v_lshlrev_b32_e32 v28, 3, v22
	v_addc_co_u32_e32 v27, vcc, 0, v5, vcc
	global_load_dwordx2 v[8:9], v[24:25], off
	global_load_dwordx2 v[6:7], v[24:25], off offset:2048
	global_load_dwordx2 v[4:5], v28, s[8:9]
	global_load_dwordx2 v[2:3], v[26:27], off offset:2048
	v_cmp_gt_i32_e32 vcc, s52, v0
	v_mov_b32_e32 v27, -1
	v_mov_b32_e32 v32, -1
	s_and_saveexec_b64 s[8:9], vcc
	s_cbranch_execz .LBB1_7
	s_waitcnt vmcnt(9)
	v_lshrrev_b32_e32 v24, 16, v20
	v_lshlrev_b32_e32 v25, 2, v24
	v_mov_b32_e32 v26, 1
	ds_add_rtn_u32 v25, v25, v26 offset:10832
	s_waitcnt lgkmcnt(0)
	v_lshl_or_b32 v32, v25, 8, v24
.LBB1_7:
	s_or_b64 exec, exec, s[8:9]
	v_or_b32_e32 v24, 0x100, v0
	v_cmp_gt_i32_e32 vcc, s53, v24
	s_and_saveexec_b64 s[8:9], vcc
	s_cbranch_execz .LBB1_9
	s_waitcnt vmcnt(8)
	v_lshrrev_b32_e32 v24, 16, v18
	v_lshlrev_b32_e32 v25, 2, v24
	v_mov_b32_e32 v26, 1
	ds_add_rtn_u32 v25, v25, v26 offset:10832
	s_waitcnt lgkmcnt(0)
	v_lshl_or_b32 v27, v25, 8, v24
.LBB1_9:
	s_or_b64 exec, exec, s[8:9]
	v_or_b32_e32 v24, 0x200, v0
	v_cmp_gt_i32_e32 vcc, s54, v24
	v_mov_b32_e32 v26, -1
	v_mov_b32_e32 v31, -1
	s_and_saveexec_b64 s[8:9], vcc
	s_cbranch_execz .LBB1_11
	s_waitcnt vmcnt(7)
	v_lshrrev_b32_e32 v24, 16, v16
	v_lshlrev_b32_e32 v25, 2, v24
	v_mov_b32_e32 v28, 1
	ds_add_rtn_u32 v25, v25, v28 offset:10832
	s_waitcnt lgkmcnt(0)
	v_lshl_or_b32 v31, v25, 8, v24
.LBB1_11:
	s_or_b64 exec, exec, s[8:9]
	v_or_b32_e32 v24, 0x300, v0
	v_cmp_gt_i32_e32 vcc, s55, v24
	s_and_saveexec_b64 s[8:9], vcc
	s_cbranch_execz .LBB1_13
	s_waitcnt vmcnt(6)
	v_lshrrev_b32_e32 v24, 16, v14
	v_lshlrev_b32_e32 v25, 2, v24
	v_mov_b32_e32 v26, 1
	ds_add_rtn_u32 v25, v25, v26 offset:10832
	s_waitcnt lgkmcnt(0)
	v_lshl_or_b32 v26, v25, 8, v24
.LBB1_13:
	s_or_b64 exec, exec, s[8:9]
	v_cmp_gt_i32_e32 vcc, s56, v23
	v_mov_b32_e32 v24, -1
	v_mov_b32_e32 v30, -1
	s_and_saveexec_b64 s[8:9], vcc
	s_cbranch_execz .LBB1_15
	s_waitcnt vmcnt(5)
	v_lshrrev_b32_e32 v23, 16, v12
	v_lshlrev_b32_e32 v25, 2, v23
	v_mov_b32_e32 v28, 1
	ds_add_rtn_u32 v25, v25, v28 offset:10832
	s_waitcnt lgkmcnt(0)
	v_lshl_or_b32 v30, v25, 8, v23
.LBB1_15:
	s_or_b64 exec, exec, s[8:9]
	v_or_b32_e32 v23, 0x500, v0
	v_cmp_gt_i32_e32 vcc, s57, v23
	s_and_saveexec_b64 s[8:9], vcc
	s_cbranch_execz .LBB1_17
	s_waitcnt vmcnt(4)
	v_lshrrev_b32_e32 v23, 16, v10
	v_lshlrev_b32_e32 v24, 2, v23
	v_mov_b32_e32 v25, 1
	ds_add_rtn_u32 v24, v24, v25 offset:10832
	s_waitcnt lgkmcnt(0)
	v_lshl_or_b32 v24, v24, 8, v23
.LBB1_17:
	s_or_b64 exec, exec, s[8:9]
	v_or_b32_e32 v23, 0x600, v0
	v_cmp_gt_i32_e32 vcc, s58, v23
	v_mov_b32_e32 v23, -1
	v_mov_b32_e32 v29, -1
	s_and_saveexec_b64 s[8:9], vcc
	s_cbranch_execz .LBB1_19
	s_waitcnt vmcnt(3)
	v_lshrrev_b32_e32 v25, 16, v8
	v_lshlrev_b32_e32 v28, 2, v25
	v_mov_b32_e32 v29, 1
	ds_add_rtn_u32 v28, v28, v29 offset:10832
	s_waitcnt lgkmcnt(0)
	v_lshl_or_b32 v29, v28, 8, v25
.LBB1_19:
	s_or_b64 exec, exec, s[8:9]
	v_or_b32_e32 v25, 0x700, v0
	v_cmp_gt_i32_e32 vcc, s59, v25
	s_and_saveexec_b64 s[8:9], vcc
	s_cbranch_execz .LBB1_21
	s_waitcnt vmcnt(2)
	v_lshrrev_b32_e32 v23, 16, v6
	v_lshlrev_b32_e32 v25, 2, v23
	v_mov_b32_e32 v28, 1
	ds_add_rtn_u32 v25, v25, v28 offset:10832
	s_waitcnt lgkmcnt(0)
	v_lshl_or_b32 v23, v25, 8, v23
.LBB1_21:
	s_or_b64 exec, exec, s[8:9]
	v_cmp_gt_i32_e32 vcc, s60, v22
	v_mov_b32_e32 v22, -1
	v_mov_b32_e32 v28, -1
	s_and_saveexec_b64 s[8:9], vcc
	s_cbranch_execz .LBB1_23
	s_waitcnt vmcnt(1)
	v_lshrrev_b32_e32 v25, 16, v4
	v_lshlrev_b32_e32 v28, 2, v25
	v_mov_b32_e32 v33, 1
	ds_add_rtn_u32 v28, v28, v33 offset:10832
	s_waitcnt lgkmcnt(0)
	v_lshl_or_b32 v28, v28, 8, v25
.LBB1_23:
	s_or_b64 exec, exec, s[8:9]
	v_or_b32_e32 v25, 0x900, v0
	v_cmp_gt_i32_e32 vcc, s61, v25
	s_and_saveexec_b64 s[8:9], vcc
	s_cbranch_execz .LBB1_25
	s_waitcnt vmcnt(0)
	v_lshrrev_b32_e32 v22, 16, v2
	v_lshlrev_b32_e32 v25, 2, v22
	v_mov_b32_e32 v33, 1
	ds_add_rtn_u32 v25, v25, v33 offset:10832
	s_waitcnt lgkmcnt(0)
	v_lshl_or_b32 v22, v25, 8, v22

	.amdhsa_kernel _Z13gather_kernelPK15HIP_vector_typeIjLj2EEPKiPK6OvfRecPKDF16_PKfPDF16_
		.amdhsa_group_segment_fixed_size 12112
		.amdhsa_private_segment_fixed_size 0
		.amdhsa_kernarg_size 48
		.amdhsa_user_sgpr_count 2
		.amdhsa_user_sgpr_dispatch_ptr 0
		.amdhsa_user_sgpr_queue_ptr 0
		.amdhsa_user_sgpr_kernarg_segment_ptr 1
		.amdhsa_user_sgpr_dispatch_id 0
		.amdhsa_user_sgpr_kernarg_preload_length 0
		.amdhsa_user_sgpr_kernarg_preload_offset 0
		.amdhsa_user_sgpr_private_segment_size 0
		.amdhsa_uses_dynamic_stack 0
		.amdhsa_enable_private_segment 0
		.amdhsa_system_sgpr_workgroup_id_x 1
		.amdhsa_system_sgpr_workgroup_id_y 0
		.amdhsa_system_sgpr_workgroup_id_z 0
		.amdhsa_system_sgpr_workgroup_info 0
		.amdhsa_system_vgpr_workitem_id 0
		.amdhsa_next_free_vgpr 63
		.amdhsa_next_free_sgpr 64
		.amdhsa_accum_offset 64
		.amdhsa_reserve_vcc 1
		.amdhsa_float_round_mode_32 0
		.amdhsa_float_round_mode_16_64 0
		.amdhsa_float_denorm_mode_32 3
		.amdhsa_float_denorm_mode_16_64 3
		.amdhsa_dx10_clamp 1
		.amdhsa_ieee_mode 1
		.amdhsa_fp16_overflow 0
		.amdhsa_tg_split 0
		.amdhsa_exception_fp_ieee_invalid_op 0
		.amdhsa_exception_fp_denorm_src 0
		.amdhsa_exception_fp_ieee_div_zero 0
		.amdhsa_exception_fp_ieee_overflow 0
		.amdhsa_exception_fp_ieee_underflow 0
		.amdhsa_exception_fp_ieee_inexact 0
		.amdhsa_exception_int_div_zero 0
	.end_amdhsa_kernel

.LBB2_14:
	s_or_b64 exec, exec, s[0:1]
	v_lshlrev_b32_e32 v0, 2, v0
	s_waitcnt lgkmcnt(0)
	s_barrier
	ds_read_b32 v1, v0
	s_lshl_b32 s0, s2, 11
	s_and_b32 s0, s0, 0x1800
	s_or_b32 s0, s0, 0x2000
	s_add_u32 s0, s12, s0
	s_addc_u32 s1, s13, 0
	s_waitcnt lgkmcnt(0)
	global_atomic_add_f32 v0, v1, s[0:1]
	ds_read_b32 v1, v0 offset:1024
	s_waitcnt lgkmcnt(0)
	global_atomic_add_f32 v0, v1, s[0:1] offset:1024
	s_endpgm
	.p2alignl 8, 3212836864

_Z11gemm_kernelILi2EEvPKDF16_S1_PKfPDF16_PfS5_S3_S3_S1_S3_:
	s_load_dwordx4 s[8:11], s[0:1], 0x28
	s_load_dwordx4 s[4:7], s[0:1], 0x0
	v_mov_b32_e32 v211, 0
	v_lshlrev_b32_e32 v178, 2, v0
	v_mov_b32_e32 v179, v211
	s_waitcnt lgkmcnt(0)
	v_lshl_add_u64 v[2:3], s[8:9], 0, v[178:179]
	s_movk_i32 s3, 0x1000
	v_add_co_u32_e32 v4, vcc, s3, v2
	s_movk_i32 s14, 0x2000
	s_nop 0
	v_addc_co_u32_e32 v5, vcc, 0, v3, vcc
	v_add_co_u32_e32 v6, vcc, s14, v2
	s_movk_i32 s15, 0x3000
	s_nop 0
	v_addc_co_u32_e32 v7, vcc, 0, v3, vcc
	global_load_dword v46, v[6:7], off
	global_load_dword v47, v[6:7], off offset:1024
	global_load_dword v48, v[6:7], off offset:2048
	global_load_dword v49, v[6:7], off offset:3072
	v_add_co_u32_e32 v2, vcc, s15, v2
	v_lshrrev_b32_e32 v1, 6, v0
	s_nop 0
	v_addc_co_u32_e32 v3, vcc, 0, v3, vcc
	global_load_dword v50, v[2:3], off
	global_load_dword v51, v[2:3], off offset:1024
	global_load_dword v52, v[2:3], off offset:2048
	global_load_dword v53, v[2:3], off offset:3072
	s_load_dwordx2 s[8:9], s[0:1], 0x48
	s_load_dwordx2 s[12:13], s[0:1], 0x38
	global_load_dword v54, v178, s[10:11]
	s_waitcnt lgkmcnt(0)
	global_load_dword v112, v178, s[8:9]
	global_load_dword v120, v178, s[12:13]
	v_lshlrev_b32_e32 v2, 4, v0
	v_and_b32_e32 v2, 0x3f0, v2
	v_lshl_or_b32 v210, v1, 15, v2
	v_lshl_add_u64 v[94:95], s[6:7], 0, v[210:211]
	v_add_co_u32_e32 v42, vcc, s3, v94
	s_movk_i32 s9, 0x4000
	s_nop 0
	v_addc_co_u32_e32 v43, vcc, 0, v95, vcc
	v_add_co_u32_e32 v34, vcc, s14, v94
	s_mov_b32 s8, 0x800000
	s_nop 0
	v_addc_co_u32_e32 v35, vcc, 0, v95, vcc
	v_add_co_u32_e32 v66, vcc, s15, v94
	s_movk_i32 s3, 0x5000
	s_nop 0
	v_addc_co_u32_e32 v67, vcc, 0, v95, vcc
	v_add_co_u32_e32 v68, vcc, s9, v94
	v_lshrrev_b32_e32 v180, 5, v0
	s_nop 0
	v_addc_co_u32_e32 v69, vcc, 0, v95, vcc
	global_load_dwordx4 v[2:5], v[42:43], off offset:1024
	global_load_dwordx4 v[6:9], v[42:43], off offset:2048
	global_load_dwordx4 v[10:13], v[34:35], off offset:-4096
	global_load_dwordx4 v[14:17], v[34:35], off
	global_load_dwordx4 v[18:21], v[34:35], off offset:1024
	global_load_dwordx4 v[22:25], v[34:35], off offset:2048
	global_load_dwordx4 v[26:29], v[34:35], off offset:3072
	global_load_dwordx4 v[30:33], v[68:69], off offset:-4096
	v_and_b32_e32 v179, 31, v0
	v_lshlrev_b32_e32 v142, 5, v179
	s_waitcnt vmcnt(18)
	v_add_f32_e32 v34, 0, v46
	s_waitcnt vmcnt(17)
	v_add_f32_e32 v35, 0, v47
	s_waitcnt vmcnt(16)
	v_add_f32_e32 v34, v34, v48
	s_waitcnt vmcnt(15)
	v_add_f32_e32 v35, v35, v49
	s_waitcnt vmcnt(14)
	v_add_f32_e32 v34, v34, v50
	s_waitcnt vmcnt(13)
	v_add_f32_e32 v35, v35, v51
	s_waitcnt vmcnt(12)
	v_add_f32_e32 v44, v34, v52
	s_waitcnt vmcnt(11)
	v_add_f32_e32 v34, v35, v53
	v_mul_f32_e32 v35, 0x37a7c5ac, v44
	v_mul_f32_e32 v34, 0x37a7c5ac, v34
	v_fma_f32 v34, -v35, v35, v34
	v_add_f32_e32 v34, 0x3727c5ac, v34
	v_mul_f32_e32 v35, 0x4b800000, v34
	v_cmp_gt_f32_e32 vcc, s8, v34
	s_waitcnt vmcnt(9)
	v_fmamk_f32 v113, v44, 0x37a7c5ac, v112
	v_cndmask_b32_e32 v34, v34, v35, vcc
	v_rsq_f32_e32 v45, v34
	global_load_dwordx4 v[34:37], v[42:43], off offset:3072
	global_load_dwordx4 v[38:41], v[66:67], off offset:1024
	v_mul_f32_e32 v42, 0x45800000, v45
	v_cndmask_b32_e32 v42, v45, v42, vcc
	v_add_co_u32_e32 v110, vcc, s3, v94
	s_movk_i32 s3, 0x6000
	s_nop 0
	v_addc_co_u32_e32 v111, vcc, 0, v95, vcc
	v_add_co_u32_e32 v96, vcc, s3, v94
	s_movk_i32 s3, 0x7000
	s_nop 0
	v_addc_co_u32_e32 v97, vcc, 0, v95, vcc
	v_add_co_u32_e32 v118, vcc, s3, v94
	v_mul_f32_e32 v121, v42, v54
	global_load_dwordx4 v[42:45], v[66:67], off offset:2048
	global_load_dwordx4 v[46:49], v[66:67], off offset:3072
	global_load_dwordx4 v[50:53], v[68:69], off
	global_load_dwordx4 v[54:57], v[68:69], off offset:1024
	global_load_dwordx4 v[58:61], v[68:69], off offset:2048
	global_load_dwordx4 v[62:65], v[68:69], off offset:3072
	s_nop 0
	global_load_dwordx4 v[66:69], v[110:111], off offset:1024
	global_load_dwordx4 v[70:73], v[110:111], off offset:2048
	global_load_dwordx4 v[74:77], v[96:97], off offset:-4096
	global_load_dwordx4 v[78:81], v[96:97], off
	global_load_dwordx4 v[82:85], v[96:97], off offset:1024
	global_load_dwordx4 v[86:89], v[96:97], off offset:2048
	global_load_dwordx4 v[90:93], v[96:97], off offset:3072
	v_addc_co_u32_e32 v119, vcc, 0, v95, vcc
	global_load_dwordx4 v[94:97], v[110:111], off offset:3072
	global_load_dwordx4 v[98:101], v[118:119], off
	global_load_dwordx4 v[102:105], v[118:119], off offset:1024
	global_load_dwordx4 v[106:109], v[118:119], off offset:2048
	v_sub_f32_e32 v110, v112, v113
	s_waitcnt vmcnt(27)
	v_fmac_f32_e32 v120, v110, v121
	global_load_dwordx4 v[110:113], v210, s[6:7]
	global_load_dwordx4 v[114:117], v[118:119], off offset:3072
	ds_write2st64_b32 v178, v121, v120 offset1:4
	global_load_dwordx4 v[118:121], v210, s[6:7] offset:1024
	global_load_dwordx4 v[122:125], v210, s[6:7] offset:2048
	global_load_dwordx4 v[126:129], v210, s[6:7] offset:3072
	s_lshl_b32 s6, s2, 5
	v_or_b32_e32 v158, s6, v180
	v_min_i32_e32 v146, 0xc34f, v158
	v_ashrrev_i32_e32 v147, 31, v146
	v_lshlrev_b64 v[146:147], 9, v[146:147]
	v_lshl_add_u64 v[146:147], s[4:5], 0, v[146:147]
	v_lshlrev_b32_e32 v210, 4, v179
	v_lshl_add_u64 v[146:147], v[146:147], 0, v[210:211]
	s_waitcnt lgkmcnt(0)
	s_barrier
	ds_read_b128 v[130:133], v142
	ds_read_b128 v[134:137], v142 offset:16
	ds_read_b128 v[138:141], v142 offset:1024
	ds_read_b128 v[142:145], v142 offset:1040
	s_waitcnt lgkmcnt(0)
	s_barrier
	global_load_dwordx4 v[146:149], v[146:147], off nt
	v_or_b32_e32 v150, 8, v158
	v_min_i32_e32 v150, 0xc34f, v150
	v_ashrrev_i32_e32 v151, 31, v150
	v_lshlrev_b64 v[150:151], 9, v[150:151]
	v_lshl_add_u64 v[150:151], s[4:5], 0, v[150:151]
	v_lshl_add_u64 v[150:151], v[150:151], 0, v[210:211]
	global_load_dwordx4 v[150:153], v[150:151], off nt
	v_or_b32_e32 v154, 16, v158
	v_min_i32_e32 v154, 0xc34f, v154
	v_ashrrev_i32_e32 v155, 31, v154
	v_lshlrev_b64 v[154:155], 9, v[154:155]
	v_lshl_add_u64 v[154:155], s[4:5], 0, v[154:155]
	v_lshl_add_u64 v[154:155], v[154:155], 0, v[210:211]
	global_load_dwordx4 v[154:157], v[154:155], off nt
	v_or_b32_e32 v158, 24, v158
	v_min_i32_e32 v158, 0xc34f, v158
	v_ashrrev_i32_e32 v159, 31, v158
	v_lshlrev_b64 v[158:159], 9, v[158:159]
	v_lshl_add_u64 v[158:159], s[4:5], 0, v[158:159]
	v_lshl_add_u64 v[158:159], v[158:159], 0, v[210:211]
	global_load_dwordx4 v[158:161], v[158:159], off nt
	s_movk_i32 s7, 0x210
	v_mad_u32_u24 v216, v180, s7, v210
	s_mov_b32 s3, 0
	s_cmpk_gt_i32 s2, 0x61a
	s_waitcnt vmcnt(3)
	v_cvt_f32_f16_e32 v162, v146
	v_cvt_f32_f16_sdwa v163, v146 dst_sel:DWORD dst_unused:UNUSED_PAD src0_sel:WORD_1
	v_cvt_f32_f16_e32 v164, v147
	v_cvt_f32_f16_sdwa v165, v147 dst_sel:DWORD dst_unused:UNUSED_PAD src0_sel:WORD_1
	v_pk_fma_f32 v[162:163], v[130:131], v[162:163], v[138:139]
	s_nop 0
	v_max_f32_e32 v166, 0, v163
	v_max_f32_e32 v167, 0, v162
	v_pk_fma_f32 v[162:163], v[132:133], v[164:165], v[140:141]
	v_cvt_f32_f16_e32 v164, v148
	v_cvt_f32_f16_sdwa v165, v148 dst_sel:DWORD dst_unused:UNUSED_PAD src0_sel:WORD_1
	v_max_f32_e32 v168, 0, v162
	v_cvt_pk_f16_f32 v162, v167, v166
	v_cvt_f32_f16_e32 v166, v149
	v_cvt_f32_f16_sdwa v167, v149 dst_sel:DWORD dst_unused:UNUSED_PAD src0_sel:WORD_1
	v_pk_fma_f32 v[164:165], v[134:135], v[164:165], v[142:143]
	v_max_f32_e32 v163, 0, v163
	v_max_f32_e32 v165, 0, v165
	v_max_f32_e32 v164, 0, v164
	v_pk_fma_f32 v[166:167], v[136:137], v[166:167], v[144:145]
	v_cvt_pk_f16_f32 v164, v164, v165
	v_max_f32_e32 v165, 0, v167
	v_max_f32_e32 v166, 0, v166
	v_cvt_pk_f16_f32 v163, v168, v163
	v_cvt_pk_f16_f32 v165, v166, v165
	s_waitcnt vmcnt(2)
	v_cvt_f32_f16_e32 v166, v150
	v_cvt_f32_f16_sdwa v167, v150 dst_sel:DWORD dst_unused:UNUSED_PAD src0_sel:WORD_1
	ds_write_b128 v216, v[162:165]
	v_cvt_f32_f16_e32 v162, v151
	v_cvt_f32_f16_sdwa v163, v151 dst_sel:DWORD dst_unused:UNUSED_PAD src0_sel:WORD_1
	v_pk_fma_f32 v[164:165], v[130:131], v[166:167], v[138:139]
	v_pk_fma_f32 v[162:163], v[132:133], v[162:163], v[140:141]
	v_max_f32_e32 v166, 0, v165
	v_max_f32_e32 v167, 0, v164
	v_cvt_f32_f16_e32 v164, v152
	v_cvt_f32_f16_sdwa v165, v152 dst_sel:DWORD dst_unused:UNUSED_PAD src0_sel:WORD_1
	v_max_f32_e32 v168, 0, v162
	v_cvt_pk_f16_f32 v162, v167, v166
	v_cvt_f32_f16_e32 v166, v153
	v_cvt_f32_f16_sdwa v167, v153 dst_sel:DWORD dst_unused:UNUSED_PAD src0_sel:WORD_1
	v_pk_fma_f32 v[164:165], v[134:135], v[164:165], v[142:143]
	v_max_f32_e32 v163, 0, v163
	v_max_f32_e32 v165, 0, v165
	v_max_f32_e32 v164, 0, v164
	v_pk_fma_f32 v[166:167], v[136:137], v[166:167], v[144:145]
	v_cvt_pk_f16_f32 v164, v164, v165
	v_max_f32_e32 v165, 0, v167
	v_max_f32_e32 v166, 0, v166
	v_cvt_pk_f16_f32 v163, v168, v163
	v_cvt_pk_f16_f32 v165, v166, v165
	s_waitcnt vmcnt(1)
	v_cvt_f32_f16_e32 v166, v154
	v_cvt_f32_f16_sdwa v167, v154 dst_sel:DWORD dst_unused:UNUSED_PAD src0_sel:WORD_1
	ds_write_b128 v216, v[162:165] offset:4224
	v_cvt_f32_f16_e32 v162, v155
	v_cvt_f32_f16_sdwa v163, v155 dst_sel:DWORD dst_unused:UNUSED_PAD src0_sel:WORD_1
	v_pk_fma_f32 v[164:165], v[130:131], v[166:167], v[138:139]
	v_pk_fma_f32 v[162:163], v[132:133], v[162:163], v[140:141]
	v_max_f32_e32 v166, 0, v165
	v_max_f32_e32 v167, 0, v164
	v_cvt_f32_f16_e32 v164, v156
	v_cvt_f32_f16_sdwa v165, v156 dst_sel:DWORD dst_unused:UNUSED_PAD src0_sel:WORD_1
	v_max_f32_e32 v168, 0, v162
	v_cvt_pk_f16_f32 v162, v167, v166
	v_cvt_f32_f16_e32 v166, v157
	v_cvt_f32_f16_sdwa v167, v157 dst_sel:DWORD dst_unused:UNUSED_PAD src0_sel:WORD_1
	v_pk_fma_f32 v[164:165], v[134:135], v[164:165], v[142:143]
	v_max_f32_e32 v163, 0, v163
	v_max_f32_e32 v165, 0, v165
	v_max_f32_e32 v164, 0, v164
	v_pk_fma_f32 v[166:167], v[136:137], v[166:167], v[144:145]
	v_cvt_pk_f16_f32 v164, v164, v165
	v_max_f32_e32 v165, 0, v167
	v_max_f32_e32 v166, 0, v166
	v_cvt_pk_f16_f32 v163, v168, v163
	v_cvt_pk_f16_f32 v165, v166, v165
	s_waitcnt vmcnt(0)
	v_cvt_f32_f16_e32 v166, v158
	v_cvt_f32_f16_sdwa v167, v158 dst_sel:DWORD dst_unused:UNUSED_PAD src0_sel:WORD_1
	ds_write_b128 v216, v[162:165] offset:8448
	v_cvt_f32_f16_e32 v162, v159
	v_cvt_f32_f16_sdwa v163, v159 dst_sel:DWORD dst_unused:UNUSED_PAD src0_sel:WORD_1
	v_pk_fma_f32 v[164:165], v[130:131], v[166:167], v[138:139]
	v_pk_fma_f32 v[162:163], v[132:133], v[162:163], v[140:141]
	v_max_f32_e32 v166, 0, v165
	v_max_f32_e32 v167, 0, v164
	v_cvt_f32_f16_e32 v164, v160
	v_cvt_f32_f16_sdwa v165, v160 dst_sel:DWORD dst_unused:UNUSED_PAD src0_sel:WORD_1
	v_max_f32_e32 v168, 0, v162
	v_cvt_pk_f16_f32 v162, v167, v166
	v_cvt_f32_f16_e32 v166, v161
	v_cvt_f32_f16_sdwa v167, v161 dst_sel:DWORD dst_unused:UNUSED_PAD src0_sel:WORD_1
	v_pk_fma_f32 v[164:165], v[134:135], v[164:165], v[142:143]
	v_max_f32_e32 v163, 0, v163
	v_max_f32_e32 v165, 0, v165
	v_max_f32_e32 v164, 0, v164
	v_pk_fma_f32 v[166:167], v[136:137], v[166:167], v[144:145]
	v_cvt_pk_f16_f32 v164, v164, v165
	v_max_f32_e32 v165, 0, v167
	v_max_f32_e32 v166, 0, v166
	v_cvt_pk_f16_f32 v163, v168, v163
	v_cvt_pk_f16_f32 v165, v166, v165
	ds_write_b128 v216, v[162:165] offset:12672
	s_waitcnt lgkmcnt(0)
	s_barrier
	s_cbranch_scc1 .LBB3_11
	v_lshrrev_b32_e32 v162, 2, v0
	s_load_dwordx2 s[10:11], s[0:1], 0x10
	s_load_dword s12, s[0:1], 0x50
	s_load_dwordx2 s[8:9], s[0:1], 0x20
	v_and_b32_e32 v181, 12, v162
	s_movk_i32 s13, 0xc0
	v_and_or_b32 v162, v0, s13, v181
	v_lshlrev_b32_e32 v174, 2, v162
	s_waitcnt lgkmcnt(0)
	global_load_dwordx4 v[162:165], v174, s[10:11]
	global_load_dwordx4 v[166:169], v174, s[10:11] offset:64
	global_load_dwordx4 v[170:173], v174, s[10:11] offset:128
	s_nop 0
	global_load_dwordx4 v[174:177], v174, s[10:11] offset:192
	s_load_dwordx2 s[0:1], s[0:1], 0x40
	v_lshlrev_b32_e32 v179, 3, v179
	v_lshlrev_b32_e32 v210, 1, v179
	v_and_b32_e32 v182, 15, v0
	v_lshl_add_u64 v[212:213], s[4:5], 0, v[210:211]
	v_and_b32_e32 v179, 48, v0
	v_mul_u32_u24_e32 v210, 0xc350, v1
	v_lshlrev_b32_e32 v0, 1, v181
	s_waitcnt lgkmcnt(0)
	s_mov_b64 s[18:19], s[0:1]
	s_add_i32 s0, s2, s12
	v_and_b32_e32 v178, 0x300, v178
	v_lshl_or_b32 v218, s0, 5, v180
	s_lshl_b32 s0, s2, 15
	v_lshlrev_b32_e32 v180, 10, v182
	v_or3_b32 v178, s0, v180, v178
	s_movk_i32 s0, 0x40c0
	s_mov_b32 s11, 0x20000
	s_mov_b32 s10, 0x30d4000
	s_and_b32 s9, s9, 0xffff
	s_mov_b32 s13, 0xc350
	v_mad_u32_u24 v217, v182, s7, v179
	s_lshl_b32 s14, s12, 5
	v_add_u32_e32 v219, s6, v182
	v_or3_b32 v220, v178, v179, s0
	s_lshl_b32 s15, s12, 15
	s_mov_b32 s16, 0
	v_add_u32_e32 v210, v210, v219
	s_lshl_b32 s17, s12, 12
	v_lshl_add_u32 v210, v210, 7, v0
	s_waitcnt vmcnt(0)
	s_branch .LBB3_3
